# adds instruction selection: indexer relu without the redundant canonicalising v_max, attention softmax mask via v_bfe_i32+v_and (2 ops instead of 3)
# speedup vs baseline: 1.0075x; 1.0075x over previous
.LBB0_409:
	v_cndmask_b32_e64 v2, 0, 1, s[0:1]
	v_cmp_ne_u32_e32 vcc, 1, v2
	v_or_b32_e32 v2, s8, v168
	v_lshlrev_b32_e32 v2, 9, v2
	v_or_b32_e32 v169, s8, v1
	v_lshl_add_u64 v[4:5], v[2:3], 2, s[2:3]
	v_mad_u32_u24 v170, v169, s91, v135
	global_load_dwordx4 v[36:39], v[4:5], off offset:336
	global_load_dwordx4 v[40:43], v[4:5], off offset:320
	ds_read_b128 v[4:7], v170
	ds_read_b128 v[52:55], v170 offset:32
	s_waitcnt lgkmcnt(1)
	v_mfma_f32_32x32x16_bf16 v[4:19], v[20:23], v[4:7], 0
	s_mov_b32 s8, 32
	s_mov_b64 s[0:1], 0
	s_and_b64 vcc, exec, vcc
	ds_read_b128 v[68:71], v170 offset:160
	ds_read_b128 v[84:87], v170 offset:288
	ds_read_b128 v[102:105], v170 offset:416
	ds_read_b128 v[118:121], v170 offset:544
	s_waitcnt lgkmcnt(4)
	v_mfma_f32_32x32x16_bf16 v[4:19], v[24:27], v[52:55], v[4:19]
	ds_read_b128 v[52:55], v170 offset:64
	ds_read_b128 v[136:139], v170 offset:672
	ds_read_b128 v[152:155], v170 offset:800
	ds_read_b128 v[172:175], v170 offset:928
	s_waitcnt vmcnt(1)
	v_mul_f32_e32 v36, 0x3d3504f3, v36
	s_waitcnt lgkmcnt(3)
	v_mfma_f32_32x32x16_bf16 v[4:19], v[28:31], v[52:55], v[4:19]
	ds_read_b128 v[52:55], v170 offset:96
	s_waitcnt vmcnt(0)
	v_mul_f32_e32 v2, 0x3d3504f3, v40
	v_mul_f32_e32 v40, 0x3d3504f3, v41
	v_mul_f32_e32 v42, 0x3d3504f3, v42
	v_mul_f32_e32 v100, 0x3d3504f3, v43
	v_mul_f32_e32 v134, 0x3d3504f3, v37
	v_mul_f32_e32 v38, 0x3d3504f3, v38
	s_waitcnt lgkmcnt(0)
	v_mfma_f32_32x32x16_bf16 v[4:19], v[32:35], v[52:55], v[4:19]
	s_nop 11
	v_max_f32_e32 v66, 0, v4
	v_max_f32_e32 v67, 0, v5
	v_max_f32_e32 v64, 0, v6
	v_max_f32_e32 v65, 0, v7
	v_max_f32_e32 v62, 0, v8
	v_max_f32_e32 v63, 0, v9
	v_max_f32_e32 v60, 0, v10
	v_max_f32_e32 v61, 0, v11
	v_max_f32_e32 v58, 0, v12
	v_max_f32_e32 v59, 0, v13
	v_max_f32_e32 v56, 0, v14
	v_max_f32_e32 v57, 0, v15
	v_max_f32_e32 v54, 0, v16
	v_max_f32_e32 v55, 0, v17
	v_max_f32_e32 v52, 0, v18
	v_max_f32_e32 v53, 0, v19
	ds_read_b128 v[4:7], v170 offset:128
	s_waitcnt lgkmcnt(0)
	v_mfma_f32_32x32x16_bf16 v[4:19], v[20:23], v[4:7], 0
	v_fma_f32 v66, v2, v66, 0
	v_fma_f32 v67, v2, v67, 0
	v_fma_f32 v64, v2, v64, 0
	v_fma_f32 v65, v2, v65, 0
	v_fma_f32 v62, v2, v62, 0
	v_fma_f32 v63, v2, v63, 0
	v_pk_fma_f32 v[60:61], v[2:3], v[60:61], 0 op_sel_hi:[0,1,0]
	v_pk_fma_f32 v[58:59], v[2:3], v[58:59], 0 op_sel_hi:[0,1,0]
	v_pk_fma_f32 v[56:57], v[2:3], v[56:57], 0 op_sel_hi:[0,1,0]
	v_pk_fma_f32 v[54:55], v[2:3], v[54:55], 0 op_sel_hi:[0,1,0]
	v_mfma_f32_32x32x16_bf16 v[4:19], v[24:27], v[68:71], v[4:19]
	ds_read_b128 v[68:71], v170 offset:192
	v_fma_f32 v52, v2, v52, 0
	v_fma_f32 v53, v2, v53, 0
	v_mul_u32_u24_e32 v2, s37, v169
	s_waitcnt lgkmcnt(0)
	v_mfma_f32_32x32x16_bf16 v[4:19], v[28:31], v[68:71], v[4:19]
	ds_read_b128 v[68:71], v170 offset:224
	s_waitcnt lgkmcnt(0)
	v_mfma_f32_32x32x16_bf16 v[4:19], v[32:35], v[68:71], v[4:19]
	s_nop 11
	v_max_f32_e32 v82, 0, v4
	v_max_f32_e32 v83, 0, v5
	v_max_f32_e32 v80, 0, v6
	v_max_f32_e32 v81, 0, v7
	v_max_f32_e32 v78, 0, v8
	v_max_f32_e32 v79, 0, v9
	v_max_f32_e32 v76, 0, v10
	v_max_f32_e32 v77, 0, v11
	v_max_f32_e32 v74, 0, v12
	v_max_f32_e32 v75, 0, v13
	v_max_f32_e32 v72, 0, v14
	v_max_f32_e32 v73, 0, v15
	v_max_f32_e32 v70, 0, v16
	v_max_f32_e32 v71, 0, v17
	v_max_f32_e32 v68, 0, v18
	v_max_f32_e32 v69, 0, v19
	ds_read_b128 v[4:7], v170 offset:256
	s_waitcnt lgkmcnt(0)
	v_mfma_f32_32x32x16_bf16 v[4:19], v[20:23], v[4:7], 0
	v_fma_f32 v66, v40, v82, v66
	v_fma_f32 v67, v40, v83, v67
	v_fma_f32 v64, v40, v80, v64
	v_fma_f32 v65, v40, v81, v65
	v_fma_f32 v62, v40, v78, v62
	v_fma_f32 v63, v40, v79, v63
	v_pk_fma_f32 v[60:61], v[40:41], v[76:77], v[60:61] op_sel_hi:[0,1,1]
	v_pk_fma_f32 v[58:59], v[40:41], v[74:75], v[58:59] op_sel_hi:[0,1,1]
	v_pk_fma_f32 v[56:57], v[40:41], v[72:73], v[56:57] op_sel_hi:[0,1,1]
	v_pk_fma_f32 v[54:55], v[40:41], v[70:71], v[54:55] op_sel_hi:[0,1,1]
	v_mfma_f32_32x32x16_bf16 v[4:19], v[24:27], v[84:87], v[4:19]
	ds_read_b128 v[84:87], v170 offset:320
	v_pk_fma_f32 v[40:41], v[40:41], v[68:69], v[52:53] op_sel_hi:[0,1,1]
	s_waitcnt lgkmcnt(0)
	v_mfma_f32_32x32x16_bf16 v[4:19], v[28:31], v[84:87], v[4:19]
	ds_read_b128 v[84:87], v170 offset:352
	s_waitcnt lgkmcnt(0)
	v_mfma_f32_32x32x16_bf16 v[4:19], v[32:35], v[84:87], v[4:19]
	s_nop 11
	v_max_f32_e32 v98, 0, v4
	v_max_f32_e32 v99, 0, v5
	v_max_f32_e32 v96, 0, v6
	v_max_f32_e32 v97, 0, v7
	v_max_f32_e32 v94, 0, v8
	v_max_f32_e32 v95, 0, v9
	v_max_f32_e32 v92, 0, v10
	v_max_f32_e32 v93, 0, v11
	v_max_f32_e32 v90, 0, v12
	v_max_f32_e32 v91, 0, v13
	v_max_f32_e32 v88, 0, v14
	v_max_f32_e32 v89, 0, v15
	v_max_f32_e32 v86, 0, v16
	v_max_f32_e32 v87, 0, v17
	v_max_f32_e32 v84, 0, v18
	v_max_f32_e32 v85, 0, v19
	ds_read_b128 v[4:7], v170 offset:384
	s_waitcnt lgkmcnt(0)
	v_mfma_f32_32x32x16_bf16 v[4:19], v[20:23], v[4:7], 0
	v_fma_f32 v66, v42, v98, v66
	v_fma_f32 v67, v42, v99, v67
	v_fma_f32 v64, v42, v96, v64
	v_fma_f32 v65, v42, v97, v65
	v_fma_f32 v62, v42, v94, v62
	v_fma_f32 v63, v42, v95, v63
	v_pk_fma_f32 v[60:61], v[42:43], v[92:93], v[60:61] op_sel_hi:[0,1,1]
	v_pk_fma_f32 v[58:59], v[42:43], v[90:91], v[58:59] op_sel_hi:[0,1,1]
	v_pk_fma_f32 v[56:57], v[42:43], v[88:89], v[56:57] op_sel_hi:[0,1,1]
	v_pk_fma_f32 v[54:55], v[42:43], v[86:87], v[54:55] op_sel_hi:[0,1,1]
	v_mfma_f32_32x32x16_bf16 v[4:19], v[24:27], v[102:105], v[4:19]
	ds_read_b128 v[102:105], v170 offset:448
	v_fma_f32 v40, v42, v84, v40
	v_fma_f32 v41, v42, v85, v41
	s_waitcnt lgkmcnt(0)
	v_mfma_f32_32x32x16_bf16 v[4:19], v[28:31], v[102:105], v[4:19]
	ds_read_b128 v[102:105], v170 offset:480
	s_waitcnt lgkmcnt(0)
	v_mfma_f32_32x32x16_bf16 v[4:19], v[32:35], v[102:105], v[4:19]
	s_nop 11
	v_max_f32_e32 v116, 0, v4
	v_max_f32_e32 v117, 0, v5
	v_max_f32_e32 v114, 0, v6
	v_max_f32_e32 v115, 0, v7
	v_max_f32_e32 v112, 0, v8
	v_max_f32_e32 v113, 0, v9
	v_max_f32_e32 v110, 0, v10
	v_max_f32_e32 v111, 0, v11
	v_max_f32_e32 v108, 0, v12
	v_max_f32_e32 v109, 0, v13
	v_max_f32_e32 v106, 0, v14
	v_max_f32_e32 v107, 0, v15
	v_max_f32_e32 v104, 0, v16
	v_max_f32_e32 v105, 0, v17
	v_max_f32_e32 v102, 0, v18
	v_max_f32_e32 v103, 0, v19
	ds_read_b128 v[4:7], v170 offset:512
	s_waitcnt lgkmcnt(0)
	v_mfma_f32_32x32x16_bf16 v[4:19], v[20:23], v[4:7], 0
	v_fma_f32 v66, v100, v116, v66
	v_fma_f32 v67, v100, v117, v67
	v_fma_f32 v64, v100, v114, v64
	v_fma_f32 v65, v100, v115, v65
	v_fma_f32 v62, v100, v112, v62
	v_fma_f32 v63, v100, v113, v63
	v_pk_fma_f32 v[60:61], v[100:101], v[110:111], v[60:61] op_sel_hi:[0,1,1]
	v_pk_fma_f32 v[58:59], v[100:101], v[108:109], v[58:59] op_sel_hi:[0,1,1]
	v_pk_fma_f32 v[56:57], v[100:101], v[106:107], v[56:57] op_sel_hi:[0,1,1]
	v_pk_fma_f32 v[54:55], v[100:101], v[104:105], v[54:55] op_sel_hi:[0,1,1]
	v_mfma_f32_32x32x16_bf16 v[4:19], v[24:27], v[118:121], v[4:19]
	ds_read_b128 v[118:121], v170 offset:576
	v_fma_f32 v40, v100, v102, v40
	v_fma_f32 v41, v100, v103, v41
	s_waitcnt lgkmcnt(0)
	v_mfma_f32_32x32x16_bf16 v[4:19], v[28:31], v[118:121], v[4:19]
	ds_read_b128 v[118:121], v170 offset:608
	s_waitcnt lgkmcnt(0)
	v_mfma_f32_32x32x16_bf16 v[4:19], v[32:35], v[118:121], v[4:19]
	s_nop 11
	v_max_f32_e32 v132, 0, v4
	v_max_f32_e32 v133, 0, v5
	v_max_f32_e32 v130, 0, v6
	v_max_f32_e32 v131, 0, v7
	v_max_f32_e32 v128, 0, v8
	v_max_f32_e32 v129, 0, v9
	v_max_f32_e32 v126, 0, v10
	v_max_f32_e32 v127, 0, v11
	v_max_f32_e32 v124, 0, v12
	v_max_f32_e32 v125, 0, v13
	v_max_f32_e32 v122, 0, v14
	v_max_f32_e32 v123, 0, v15
	v_max_f32_e32 v120, 0, v16
	v_max_f32_e32 v121, 0, v17
	v_max_f32_e32 v118, 0, v18
	v_max_f32_e32 v119, 0, v19
	ds_read_b128 v[4:7], v170 offset:640
	s_waitcnt lgkmcnt(0)
	v_mfma_f32_32x32x16_bf16 v[4:19], v[20:23], v[4:7], 0
	v_fma_f32 v66, v36, v132, v66
	v_fma_f32 v67, v36, v133, v67
	v_fma_f32 v64, v36, v130, v64
	v_fma_f32 v65, v36, v131, v65
	v_fma_f32 v62, v36, v128, v62
	v_fma_f32 v63, v36, v129, v63
	v_pk_fma_f32 v[60:61], v[36:37], v[126:127], v[60:61] op_sel_hi:[0,1,1]
	v_pk_fma_f32 v[58:59], v[36:37], v[124:125], v[58:59] op_sel_hi:[0,1,1]
	v_pk_fma_f32 v[56:57], v[36:37], v[122:123], v[56:57] op_sel_hi:[0,1,1]
	v_pk_fma_f32 v[54:55], v[36:37], v[120:121], v[54:55] op_sel_hi:[0,1,1]
	v_mfma_f32_32x32x16_bf16 v[4:19], v[24:27], v[136:139], v[4:19]
	ds_read_b128 v[136:139], v170 offset:704
	v_pk_fma_f32 v[36:37], v[36:37], v[118:119], v[40:41] op_sel_hi:[0,1,1]
	s_waitcnt lgkmcnt(0)
	v_mfma_f32_32x32x16_bf16 v[4:19], v[28:31], v[136:139], v[4:19]
	ds_read_b128 v[136:139], v170 offset:736
	s_waitcnt lgkmcnt(0)
	v_mfma_f32_32x32x16_bf16 v[4:19], v[32:35], v[136:139], v[4:19]
	s_nop 11
	v_max_f32_e32 v150, 0, v4
	v_max_f32_e32 v151, 0, v5
	v_max_f32_e32 v148, 0, v6
	v_max_f32_e32 v149, 0, v7
	v_max_f32_e32 v146, 0, v8
	v_max_f32_e32 v147, 0, v9
	v_max_f32_e32 v144, 0, v10
	v_max_f32_e32 v145, 0, v11
	v_max_f32_e32 v142, 0, v12
	v_max_f32_e32 v143, 0, v13
	v_max_f32_e32 v140, 0, v14
	v_max_f32_e32 v141, 0, v15
	v_max_f32_e32 v138, 0, v16
	v_max_f32_e32 v139, 0, v17
	v_max_f32_e32 v136, 0, v18
	v_max_f32_e32 v137, 0, v19
	ds_read_b128 v[4:7], v170 offset:768
	s_waitcnt lgkmcnt(0)
	v_mfma_f32_32x32x16_bf16 v[4:19], v[20:23], v[4:7], 0
	v_fma_f32 v66, v134, v150, v66
	v_fma_f32 v67, v134, v151, v67
	v_fma_f32 v64, v134, v148, v64
	v_fma_f32 v65, v134, v149, v65
	v_fma_f32 v36, v134, v136, v36
	v_fma_f32 v37, v134, v137, v37
	v_pk_fma_f32 v[62:63], v[134:135], v[146:147], v[62:63] op_sel_hi:[0,1,1]
	v_pk_fma_f32 v[60:61], v[134:135], v[144:145], v[60:61] op_sel_hi:[0,1,1]
	v_pk_fma_f32 v[58:59], v[134:135], v[142:143], v[58:59] op_sel_hi:[0,1,1]
	v_pk_fma_f32 v[56:57], v[134:135], v[140:141], v[56:57] op_sel_hi:[0,1,1]
	v_mfma_f32_32x32x16_bf16 v[4:19], v[24:27], v[152:155], v[4:19]
	ds_read_b128 v[152:155], v170 offset:832
	v_fma_f32 v54, v134, v138, v54
	v_fma_f32 v55, v134, v139, v55
	s_waitcnt lgkmcnt(0)
	v_mfma_f32_32x32x16_bf16 v[4:19], v[28:31], v[152:155], v[4:19]
	ds_read_b128 v[152:155], v170 offset:864
	s_waitcnt lgkmcnt(0)
	v_mfma_f32_32x32x16_bf16 v[4:19], v[32:35], v[152:155], v[4:19]
	s_nop 11
	v_max_f32_e32 v166, 0, v4
	v_max_f32_e32 v167, 0, v5
	v_max_f32_e32 v164, 0, v6
	v_max_f32_e32 v165, 0, v7
	v_max_f32_e32 v162, 0, v8
	v_max_f32_e32 v163, 0, v9
	v_max_f32_e32 v160, 0, v10
	v_max_f32_e32 v161, 0, v11
	v_max_f32_e32 v158, 0, v12
	v_max_f32_e32 v159, 0, v13
	v_max_f32_e32 v156, 0, v14
	v_max_f32_e32 v157, 0, v15
	v_max_f32_e32 v154, 0, v16
	v_max_f32_e32 v155, 0, v17
	v_max_f32_e32 v152, 0, v18
	v_max_f32_e32 v153, 0, v19
	ds_read_b128 v[4:7], v170 offset:896
	s_waitcnt lgkmcnt(0)
	v_mfma_f32_32x32x16_bf16 v[4:19], v[20:23], v[4:7], 0
	v_fma_f32 v66, v38, v166, v66
	v_fma_f32 v67, v38, v167, v67
	v_fma_f32 v64, v38, v164, v64
	v_fma_f32 v65, v38, v165, v65
	v_fma_f32 v36, v38, v152, v36
	v_fma_f32 v37, v38, v153, v37
	v_pk_fma_f32 v[62:63], v[38:39], v[162:163], v[62:63] op_sel_hi:[0,1,1]
	v_pk_fma_f32 v[60:61], v[38:39], v[160:161], v[60:61] op_sel_hi:[0,1,1]
	v_pk_fma_f32 v[58:59], v[38:39], v[158:159], v[58:59] op_sel_hi:[0,1,1]
	v_pk_fma_f32 v[56:57], v[38:39], v[156:157], v[56:57] op_sel_hi:[0,1,1]
	v_mfma_f32_32x32x16_bf16 v[4:19], v[24:27], v[172:175], v[4:19]
	ds_read_b128 v[172:175], v170 offset:960
	v_fma_f32 v54, v38, v154, v54
	v_fma_f32 v55, v38, v155, v55
	s_waitcnt lgkmcnt(0)
	v_mfma_f32_32x32x16_bf16 v[4:19], v[28:31], v[172:175], v[4:19]
	ds_read_b128 v[170:173], v170 offset:992
	s_waitcnt lgkmcnt(0)
	v_mfma_f32_32x32x16_bf16 v[4:19], v[32:35], v[170:173], v[4:19]
	v_mul_f32_e32 v170, 0x3d3504f3, v39
	s_nop 10
	v_max_f32_e32 v4, 0, v4
	v_max_f32_e32 v5, 0, v5
	v_max_f32_e32 v6, 0, v6
	v_max_f32_e32 v7, 0, v7
	v_max_f32_e32 v18, 0, v18
	v_max_f32_e32 v19, 0, v19
	v_pk_fma_f32 v[4:5], v[170:171], v[4:5], v[66:67] op_sel_hi:[0,1,1]
	v_pk_fma_f32 v[6:7], v[170:171], v[6:7], v[64:65] op_sel_hi:[0,1,1]
	v_max_f32_e32 v8, 0, v8
	v_max_f32_e32 v9, 0, v9
	v_max_f32_e32 v10, 0, v10
	v_max_f32_e32 v11, 0, v11
	v_max_f32_e32 v12, 0, v12
	v_max_f32_e32 v13, 0, v13
	v_max_f32_e32 v14, 0, v14
	v_max_f32_e32 v15, 0, v15
	v_max_f32_e32 v16, 0, v16
	v_max_f32_e32 v17, 0, v17
	v_pk_fma_f32 v[18:19], v[170:171], v[18:19], v[36:37] op_sel_hi:[0,1,1]
	v_lshl_add_u64 v[36:37], v[2:3], 2, v[50:51]
	v_pk_fma_f32 v[8:9], v[170:171], v[8:9], v[62:63] op_sel_hi:[0,1,1]
	v_pk_fma_f32 v[10:11], v[170:171], v[10:11], v[60:61] op_sel_hi:[0,1,1]
	v_pk_fma_f32 v[12:13], v[170:171], v[12:13], v[58:59] op_sel_hi:[0,1,1]
	v_pk_fma_f32 v[14:15], v[170:171], v[14:15], v[56:57] op_sel_hi:[0,1,1]
	v_pk_fma_f32 v[16:17], v[170:171], v[16:17], v[54:55] op_sel_hi:[0,1,1]
	global_store_dwordx4 v[36:37], v[4:7], off
	global_store_dwordx4 v[36:37], v[8:11], off offset:32
	global_store_dwordx4 v[36:37], v[12:15], off offset:64
	global_store_dwordx4 v[36:37], v[16:19], off offset:96
	s_cbranch_vccz .LBB0_409
	s_add_i32 s7, s7, 8
	s_cmp_ge_i32 s7, s6
	s_cbranch_scc0 .LBB0_408

.LBB0_527:
	s_mov_b32 s8, 0x3e0293ee
	v_fma_f32 v84, v84, s8, -v2
	v_exp_f32_e32 v84, v84
	v_fma_f32 v85, v85, s8, -v2
	v_lshrrev_b32_e32 v176, v171, v176
	v_exp_f32_e32 v85, v85
	v_fma_f32 v86, v86, s8, -v2
	v_bfe_i32 v250, v176, 0, 1
	v_exp_f32_e32 v86, v86
	v_fma_f32 v87, v87, s8, -v2
	v_bfe_i32 v251, v176, 1, 1
	v_exp_f32_e32 v87, v87
	v_fma_f32 v88, v88, s8, -v2
	v_and_b32_e32 v84, v84, v250
	v_bfe_i32 v250, v176, 2, 1
	v_exp_f32_e32 v88, v88
	v_fma_f32 v89, v89, s8, -v2
	v_add_f32_e32 v185, 0, v84
	v_and_b32_e32 v85, v85, v251
	v_bfe_i32 v251, v176, 3, 1
	v_exp_f32_e32 v89, v89
	v_fma_f32 v90, v90, s8, -v2
	v_add_f32_e32 v185, v85, v185
	v_and_b32_e32 v86, v86, v250
	v_bfe_i32 v250, v176, 8, 1
	v_exp_f32_e32 v90, v90
	v_fma_f32 v91, v91, s8, -v2
	v_add_f32_e32 v185, v86, v185
	v_and_b32_e32 v87, v87, v251
	v_bfe_i32 v251, v176, 9, 1
	v_exp_f32_e32 v91, v91
	v_fma_f32 v92, v92, s8, -v2
	v_add_f32_e32 v185, v87, v185
	v_and_b32_e32 v88, v88, v250
	v_bfe_i32 v250, v176, 10, 1
	v_exp_f32_e32 v92, v92
	v_fma_f32 v93, v93, s8, -v2
	v_add_f32_e32 v185, v88, v185
	v_and_b32_e32 v89, v89, v251
	v_bfe_i32 v251, v176, 11, 1
	v_exp_f32_e32 v93, v93
	v_fma_f32 v94, v94, s8, -v2
	v_add_f32_e32 v185, v89, v185
	v_and_b32_e32 v90, v90, v250
	v_bfe_i32 v250, v176, 16, 1
	v_exp_f32_e32 v94, v94
	v_fma_f32 v95, v95, s8, -v2
	v_add_f32_e32 v185, v90, v185
	v_and_b32_e32 v91, v91, v251
	v_bfe_i32 v251, v176, 17, 1
	v_exp_f32_e32 v95, v95
	v_fma_f32 v96, v96, s8, -v2
	v_add_f32_e32 v185, v91, v185
	v_and_b32_e32 v92, v92, v250
	v_bfe_i32 v250, v176, 18, 1
	v_exp_f32_e32 v96, v96
	v_fma_f32 v97, v97, s8, -v2
	v_add_f32_e32 v185, v92, v185
	v_and_b32_e32 v93, v93, v251
	v_bfe_i32 v251, v176, 19, 1
	v_exp_f32_e32 v97, v97
	v_fma_f32 v98, v98, s8, -v2
	v_add_f32_e32 v185, v93, v185
	v_and_b32_e32 v94, v94, v250
	v_bfe_i32 v250, v176, 24, 1
	v_exp_f32_e32 v98, v98
	v_fma_f32 v99, v99, s8, -v2
	v_add_f32_e32 v185, v94, v185
	v_and_b32_e32 v95, v95, v251
	v_bfe_i32 v251, v176, 25, 1
	v_exp_f32_e32 v99, v99
	v_add_f32_e32 v185, v95, v185
	v_and_b32_e32 v96, v96, v250
	v_bfe_i32 v250, v176, 26, 1
	v_add_f32_e32 v185, v96, v185
	v_and_b32_e32 v97, v97, v251
	v_bfe_i32 v251, v176, 27, 1
	v_fma_f32 v68, v68, s8, -v2
	v_add_f32_e32 v185, v97, v185
	v_and_b32_e32 v98, v98, v250
	v_exp_f32_e32 v68, v68
	v_add_f32_e32 v185, v98, v185
	v_and_b32_e32 v99, v99, v251
	v_lshrrev_b32_e32 v177, v171, v177
	v_add_f32_e32 v176, v99, v185
	v_bfe_i32 v250, v177, 0, 1
	v_fma_f32 v69, v69, s8, -v2
	v_exp_f32_e32 v69, v69
	s_mulk_i32 s7, 0x5000
	v_and_b32_e32 v185, v68, v250
	v_bfe_i32 v251, v177, 1, 1
	v_fma_f32 v68, v70, s8, -v2
	v_exp_f32_e32 v68, v68
	v_and_b32_e32 v186, v69, v251
	v_bfe_i32 v250, v177, 2, 1
	v_fma_f32 v70, v71, s8, -v2
	v_exp_f32_e32 v70, v70
	v_and_b32_e32 v187, v68, v250
	v_bfe_i32 v251, v177, 3, 1
	v_fma_f32 v68, v72, s8, -v2
	v_exp_f32_e32 v68, v68
	v_bfe_i32 v250, v177, 8, 1
	v_and_b32_e32 v188, v70, v251
	v_fma_f32 v70, v73, s8, -v2
	v_exp_f32_e32 v70, v70
	v_and_b32_e32 v189, v68, v250
	v_bfe_i32 v251, v177, 9, 1
	v_fma_f32 v68, v74, s8, -v2
	v_exp_f32_e32 v68, v68
	v_bfe_i32 v250, v177, 10, 1
	v_and_b32_e32 v190, v70, v251
	v_fma_f32 v70, v75, s8, -v2
	v_exp_f32_e32 v70, v70
	v_and_b32_e32 v191, v68, v250
	v_bfe_i32 v251, v177, 11, 1
	v_fma_f32 v68, v76, s8, -v2
	v_exp_f32_e32 v68, v68
	v_bfe_i32 v250, v177, 16, 1
	v_and_b32_e32 v192, v70, v251
	v_fma_f32 v70, v77, s8, -v2
	v_exp_f32_e32 v70, v70
	v_and_b32_e32 v193, v68, v250
	v_bfe_i32 v251, v177, 17, 1
	v_fma_f32 v68, v78, s8, -v2
	v_exp_f32_e32 v68, v68
	v_bfe_i32 v250, v177, 18, 1
	v_and_b32_e32 v194, v70, v251
	v_fma_f32 v70, v79, s8, -v2
	v_exp_f32_e32 v70, v70
	v_and_b32_e32 v195, v68, v250
	v_bfe_i32 v251, v177, 19, 1
	v_fma_f32 v68, v80, s8, -v2
	v_exp_f32_e32 v68, v68
	v_bfe_i32 v250, v177, 24, 1
	v_and_b32_e32 v196, v70, v251
	v_fma_f32 v70, v81, s8, -v2
	v_exp_f32_e32 v70, v70
	v_and_b32_e32 v197, v68, v250
	v_bfe_i32 v251, v177, 25, 1
	v_fma_f32 v68, v82, s8, -v2
	v_exp_f32_e32 v68, v68
	v_add_f32_e32 v176, v185, v176
	v_bfe_i32 v250, v177, 26, 1
	v_add_f32_e32 v176, v186, v176
	v_and_b32_e32 v198, v70, v251
	v_add_f32_e32 v176, v187, v176
	v_add_f32_e32 v176, v188, v176
	v_and_b32_e32 v199, v68, v250
	v_bfe_i32 v251, v177, 27, 1
	v_add_u32_e32 v177, s7, v180
	v_fma_f32 v2, v83, s8, -v2
	ds_read_b64_tr_b16 v[68:69], v177 offset:34816
	ds_read_b64_tr_b16 v[72:73], v177 offset:34880
	ds_read_b64_tr_b16 v[76:77], v177 offset:34944
	ds_read_b64_tr_b16 v[80:81], v177 offset:35008
	ds_read_b64_tr_b16 v[70:71], v177 offset:37376
	ds_read_b64_tr_b16 v[74:75], v177 offset:37440
	ds_read_b64_tr_b16 v[78:79], v177 offset:37504
	ds_read_b64_tr_b16 v[82:83], v177 offset:37568
	v_add_f32_e32 v176, v189, v176
	v_add_f32_e32 v176, v190, v176
	v_add_f32_e32 v176, v191, v176
	v_add_f32_e32 v176, v192, v176
	v_add_f32_e32 v176, v193, v176
	v_add_f32_e32 v176, v194, v176
	v_exp_f32_e32 v2, v2
	v_add_f32_e32 v176, v195, v176
	v_add_f32_e32 v176, v196, v176
	v_add_f32_e32 v176, v197, v176
	v_add_f32_e32 v176, v198, v176
	v_and_b32_e32 v2, v2, v251
	v_add_f32_e32 v176, v199, v176
	v_add_f32_e32 v176, v2, v176
	v_cvt_pk_bf16_f32 v84, v84, v85
	v_cvt_pk_bf16_f32 v85, v86, v87
	v_cvt_pk_bf16_f32 v86, v88, v89
	v_cvt_pk_bf16_f32 v87, v90, v91
	s_waitcnt lgkmcnt(3)
	s_nop 0
	v_mfma_f32_32x32x16_bf16 v[52:67], v[68:71], v[84:87], v[52:67]
	s_waitcnt lgkmcnt(2)
	v_mfma_f32_32x32x16_bf16 v[36:51], v[72:75], v[84:87], v[36:51]
	s_waitcnt lgkmcnt(1)
	v_mfma_f32_32x32x16_bf16 v[20:35], v[76:79], v[84:87], v[20:35]
	ds_read_b64_tr_b16 v[68:69], v177 offset:39936
	ds_read_b64_tr_b16 v[72:73], v177 offset:40000
	ds_read_b64_tr_b16 v[76:77], v177 offset:40064
	ds_read_b64_tr_b16 v[88:89], v177 offset:40128
	ds_read_b64_tr_b16 v[70:71], v177 offset:42496
	ds_read_b64_tr_b16 v[74:75], v177 offset:42560
	ds_read_b64_tr_b16 v[78:79], v177 offset:42624
	ds_read_b64_tr_b16 v[90:91], v177 offset:42688
	s_waitcnt lgkmcnt(8)
	v_mfma_f32_32x32x16_bf16 v[4:19], v[80:83], v[84:87], v[4:19]
	v_cvt_pk_bf16_f32 v80, v92, v93
	v_cvt_pk_bf16_f32 v81, v94, v95
	v_cvt_pk_bf16_f32 v82, v96, v97
	v_cvt_pk_bf16_f32 v83, v98, v99
	s_waitcnt lgkmcnt(3)
	s_nop 0
	v_mfma_f32_32x32x16_bf16 v[52:67], v[68:71], v[80:83], v[52:67]
	s_waitcnt lgkmcnt(2)
	v_mfma_f32_32x32x16_bf16 v[36:51], v[72:75], v[80:83], v[36:51]
	s_waitcnt lgkmcnt(1)
	v_mfma_f32_32x32x16_bf16 v[20:35], v[76:79], v[80:83], v[20:35]
	ds_read_b64_tr_b16 v[68:69], v177 offset:45056
	ds_read_b64_tr_b16 v[72:73], v177 offset:45120
	ds_read_b64_tr_b16 v[76:77], v177 offset:45184
	ds_read_b64_tr_b16 v[84:85], v177 offset:45248
	ds_read_b64_tr_b16 v[70:71], v177 offset:47616
	ds_read_b64_tr_b16 v[74:75], v177 offset:47680
	ds_read_b64_tr_b16 v[78:79], v177 offset:47744
	ds_read_b64_tr_b16 v[86:87], v177 offset:47808
	s_waitcnt lgkmcnt(8)
	v_mfma_f32_32x32x16_bf16 v[4:19], v[88:91], v[80:83], v[4:19]
	v_cvt_pk_bf16_f32 v80, v185, v186
	v_cvt_pk_bf16_f32 v81, v187, v188
	v_cvt_pk_bf16_f32 v82, v189, v190
	v_cvt_pk_bf16_f32 v83, v191, v192
	s_waitcnt lgkmcnt(3)
	s_nop 0
	v_mfma_f32_32x32x16_bf16 v[52:67], v[68:71], v[80:83], v[52:67]
	s_waitcnt lgkmcnt(2)
	v_mfma_f32_32x32x16_bf16 v[36:51], v[72:75], v[80:83], v[36:51]
	s_waitcnt lgkmcnt(1)
	v_mfma_f32_32x32x16_bf16 v[20:35], v[76:79], v[80:83], v[20:35]
	ds_read_b64_tr_b16 v[68:69], v177 offset:50176
	ds_read_b64_tr_b16 v[72:73], v177 offset:50240
	ds_read_b64_tr_b16 v[76:77], v177 offset:50304
	ds_read_b64_tr_b16 v[88:89], v177 offset:50368
	ds_read_b64_tr_b16 v[70:71], v177 offset:52736
	ds_read_b64_tr_b16 v[74:75], v177 offset:52800
	ds_read_b64_tr_b16 v[78:79], v177 offset:52864
	ds_read_b64_tr_b16 v[90:91], v177 offset:52928
	s_waitcnt lgkmcnt(8)
	v_mfma_f32_32x32x16_bf16 v[4:19], v[84:87], v[80:83], v[4:19]
	v_cvt_pk_bf16_f32 v80, v193, v194
	v_cvt_pk_bf16_f32 v81, v195, v196
	v_cvt_pk_bf16_f32 v82, v197, v198
	v_cvt_pk_bf16_f32 v83, v199, v2
	v_add_f32_e32 v183, v183, v176
	s_waitcnt lgkmcnt(3)
	v_mfma_f32_32x32x16_bf16 v[52:67], v[68:71], v[80:83], v[52:67]
	s_waitcnt lgkmcnt(2)
	v_mfma_f32_32x32x16_bf16 v[36:51], v[72:75], v[80:83], v[36:51]
	s_waitcnt lgkmcnt(1)
	v_mfma_f32_32x32x16_bf16 v[20:35], v[76:79], v[80:83], v[20:35]
	s_waitcnt lgkmcnt(0)
	v_mfma_f32_32x32x16_bf16 v[4:19], v[88:91], v[80:83], v[4:19]
